# v35 + weight-prep transpose items rotated by 32 workgroups so the SSM-matrix workgroups do not also carry transpose items
# speedup vs baseline: 1.0046x; 1.0046x over previous
.LBB0_1512:
	s_add_i32 s2, s45, 0xffffffe0
.Lrot_l:
	s_cmp_gt_i32 s2, -1
	s_cbranch_scc1 .Lrot_ok
	s_add_i32 s2, s2, s33
	s_branch .Lrot_l
.Lrot_ok:
	s_lshl_b32 s2, s2, 3
	s_add_i32 s30, s44, s2
	s_waitcnt lgkmcnt(0)
	v_readfirstlane_b32 s2, v5
	s_cmpk_gt_i32 s30, 0x37f
	v_readfirstlane_b32 s3, v4
	s_cbranch_scc1 .LBB0_1587
	s_lshl_b32 s31, s33, 3
	s_lshl_b64 s[0:1], s[0:1], 2
	v_lshlrev_b32_e32 v2, 3, v23
	s_add_u32 s0, s3, s0
	v_and_b32_e32 v2, 56, v2
	s_addc_u32 s1, s2, s1
	s_lshl_b32 s22, s44, 14
	v_mul_u32_u24_e32 v6, 0x84, v2
	v_lshlrev_b32_e32 v2, 1, v2
	s_add_i32 s2, s22, 0
	v_lshl_add_u64 v[4:5], s[20:21], 0, v[2:3]
	s_mov_b64 s[4:5], 0x1d00000
	v_lshl_add_u64 v[68:69], v[4:5], 0, s[4:5]
	s_add_u32 s4, s20, 0x21e0000
	s_addc_u32 s5, s21, 0
	s_lshl_b64 s[6:7], s[92:93], 22
	s_add_u32 s8, s20, 0x3d200000
	v_lshrrev_b32_e32 v80, 3, v23
	s_addc_u32 s9, s21, 0
	v_lshlrev_b32_e32 v2, 2, v80
	s_add_u32 s10, s20, 0x1de0400
	v_add3_u32 v81, s2, v6, v2
	v_lshlrev_b32_e32 v2, 2, v22
	s_addc_u32 s11, s21, 0
	s_lshl_b64 s[12:13], s[92:93], 21
	v_and_b32_e32 v70, 60, v2
	s_add_u32 s14, s20, 0x1de0000
	v_lshrrev_b32_e32 v71, 5, v23
	s_addc_u32 s15, s21, 0
	s_lshl_b32 s2, s92, 7
	v_lshlrev_b32_e32 v2, 2, v70
	v_and_b32_e32 v1, 31, v22
	s_add_u32 s16, s20, 0x1d60000
	v_lshl_add_u64 v[72:73], s[0:1], 0, v[2:3]
	v_mul_u32_u24_e32 v2, 0x84, v71
	s_addc_u32 s17, s21, 0
	s_lshl_b64 s[18:19], s[92:93], 19
	v_or_b32_e32 v2, s22, v2
	v_lshlrev_b32_e32 v4, 2, v1
	v_readlane_b32 s0, v255, 6
	v_and_b32_e32 v85, 48, v22
	s_mov_b32 s3, s93
	s_add_u32 s20, s20, 0x1200000
	v_add3_u32 v90, v2, v4, 0
	v_lshlrev_b32_e32 v2, 2, v71
	v_readlane_b32 s1, v255, 7
	v_or_b32_e32 v82, 8, v80
	v_or_b32_e32 v83, 16, v80
	v_or_b32_e32 v84, 24, v80
	s_addc_u32 s21, s21, 0
	v_or_b32_e32 v86, 0xfffff780, v85
	v_or_b32_e32 v87, 0xfffffdc0, v85
	v_or_b32_e32 v88, 0xfffffd80, v85
	v_or_b32_e32 v89, 0xffffff80, v85
	v_or_b32_e32 v91, 14, v71
	v_or_b32_e32 v92, 12, v71
	v_or_b32_e32 v93, 10, v71
	v_lshl_add_u64 v[74:75], s[0:1], 0, v[2:3]
	v_or_b32_e32 v94, 8, v71
	v_or_b32_e32 v95, 2, v71
	v_or_b32_e32 v96, 6, v71
	v_or_b32_e32 v97, 4, v71
	s_lshl_b64 s[22:23], s[2:3], 2
	s_mov_b32 s26, 0xc000
	s_movk_i32 s27, 0x5680
	s_branch .LBB0_1515
